# CMP2 (compression MLP 2nd layer) inner loop: position-term and w2-fragment global loads issued as batches into unused VGPRs instead of one at a time behind s_waitcnt (about 35 -> 2 dependent round tri
# baseline (speedup 1.0000x reference)
.LBB0_511:
	v_lshl_add_u64 v[76:77], s[86:87], 0, v[54:55]
	v_add_co_u32_e32 v78, vcc, s48, v76
	v_lshl_add_u64 v[38:39], s[86:87], 0, v[58:59]
	s_nop 0
	v_addc_co_u32_e32 v79, vcc, 0, v77, vcc
	v_add_co_u32_e32 v74, vcc, s49, v76
	v_lshl_add_u64 v[82:83], s[86:87], 0, v[60:61]
	s_nop 0
	v_addc_co_u32_e32 v75, vcc, 0, v77, vcc
	v_lshl_add_u64 v[186:187], s[86:87], 0, v[56:57]
	v_add_co_u32_e32 v188, vcc, s52, v186
	s_nop 1
	v_addc_co_u32_e32 v189, vcc, 0, v187, vcc
	v_add_co_u32_e32 v190, vcc, s53, v186
	s_nop 1
	v_addc_co_u32_e32 v191, vcc, 0, v187, vcc
	v_add_co_u32_e32 v192, vcc, s54, v186
	s_nop 1
	v_addc_co_u32_e32 v193, vcc, 0, v187, vcc
	v_add_co_u32_e32 v194, vcc, s55, v186
	s_nop 1
	v_addc_co_u32_e32 v195, vcc, 0, v187, vcc
	v_add_co_u32_e32 v196, vcc, s56, v186
	s_nop 1
	v_addc_co_u32_e32 v197, vcc, 0, v187, vcc
	v_add_co_u32_e32 v198, vcc, s57, v186
	s_nop 1
	v_addc_co_u32_e32 v199, vcc, 0, v187, vcc
	v_add_co_u32_e32 v200, vcc, s58, v186
	s_nop 1
	v_addc_co_u32_e32 v201, vcc, 0, v187, vcc
	v_add_co_u32_e32 v202, vcc, s59, v186
	s_nop 1
	v_addc_co_u32_e32 v203, vcc, 0, v187, vcc
	global_load_dwordx4 v[154:157], v[188:189], off
	s_nop 0
	global_load_dwordx4 v[158:161], v[190:191], off
	s_nop 0
	global_load_dwordx4 v[162:165], v[192:193], off
	s_nop 0
	global_load_dwordx4 v[166:169], v[194:195], off
	s_nop 0
	global_load_dwordx4 v[170:173], v[196:197], off
	s_nop 0
	global_load_dwordx4 v[174:177], v[198:199], off
	s_nop 0
	global_load_dwordx4 v[178:181], v[200:201], off
	s_nop 0
	global_load_dwordx4 v[182:185], v[202:203], off
	s_nop 0
	global_load_dwordx4 v[34:37], v[38:39], off offset:-112
	global_load_dwordx4 v[62:65], v[38:39], off offset:-128
	global_load_dwordx4 v[66:69], v[82:83], off offset:-112
	global_load_dwordx4 v[70:73], v[82:83], off offset:-128
	v_lshl_add_u64 v[40:41], v[76:77], 0, s[2:3]
	global_load_dwordx4 v[84:87], v[74:75], off offset:-4096
	global_load_dwordx4 v[88:91], v[40:41], off offset:16
	v_lshl_add_u64 v[92:93], v[76:77], 0, s[6:7]
	v_lshl_add_u64 v[96:97], v[76:77], 0, s[8:9]
	v_lshl_add_u64 v[100:101], v[76:77], 0, s[10:11]
	v_lshl_add_u64 v[104:105], v[76:77], 0, s[12:13]
	v_lshl_add_u64 v[108:109], v[76:77], 0, s[14:15]
	v_lshl_add_u64 v[112:113], v[76:77], 0, s[16:17]
	v_lshl_add_u64 v[116:117], v[76:77], 0, s[18:19]
	v_lshl_add_u64 v[122:123], v[76:77], 0, s[34:35]
	global_load_dwordx4 v[126:129], v[78:79], off offset:1024
	s_nop 0
	global_load_dwordx4 v[92:95], v[92:93], off offset:16
	s_nop 0
	global_load_dwordx4 v[130:133], v[78:79], off offset:2048
	s_nop 0
	global_load_dwordx4 v[96:99], v[96:97], off offset:16
	s_nop 0
	global_load_dwordx4 v[134:137], v[78:79], off offset:3072
	s_nop 0
	global_load_dwordx4 v[100:103], v[100:101], off offset:16
	s_nop 0
	global_load_dwordx4 v[138:141], v[74:75], off
	s_nop 0
	global_load_dwordx4 v[104:107], v[104:105], off offset:16
	s_nop 0
	global_load_dwordx4 v[142:145], v[74:75], off offset:1024
	s_nop 0
	global_load_dwordx4 v[108:111], v[108:109], off offset:16
	s_nop 0
	global_load_dwordx4 v[146:149], v[74:75], off offset:2048
	s_nop 0
	global_load_dwordx4 v[112:115], v[112:113], off offset:16
	s_nop 0
	global_load_dwordx4 v[150:153], v[74:75], off offset:3072
	s_nop 0
	global_load_dwordx4 v[116:119], v[116:117], off offset:16
	s_nop 0
	s_waitcnt vmcnt(0)
	s_add_i32 s43, s43, -2
	v_lshl_add_u64 v[54:55], v[54:55], 0, s[38:39]
	v_lshl_add_u64 v[58:59], v[58:59], 0, s[38:39]
	v_lshl_add_u64 v[60:61], v[60:61], 0, s[38:39]
	s_cmp_eq_u32 s43, 0
	v_pk_add_f32 v[34:35], v[34:35], v[66:67]
	v_pk_add_f32 v[62:63], v[62:63], v[70:71]
	v_pk_add_f32 v[40:41], v[86:87], 0 op_sel_hi:[1,0]
	v_pk_add_f32 v[80:81], v[84:85], 0 op_sel_hi:[1,0]
	v_pk_add_f32 v[64:65], v[64:65], v[72:73]
	v_pk_add_f32 v[36:37], v[36:37], v[68:69]
	v_pk_add_f32 v[40:41], v[40:41], v[128:129]
	v_pk_add_f32 v[80:81], v[80:81], v[126:127]
	v_pk_add_f32 v[40:41], v[40:41], v[132:133]
	v_pk_add_f32 v[80:81], v[80:81], v[130:131]
	v_pk_add_f32 v[40:41], v[40:41], v[136:137]
	v_pk_add_f32 v[80:81], v[80:81], v[134:135]
	v_pk_add_f32 v[40:41], v[40:41], v[140:141]
	v_pk_add_f32 v[80:81], v[80:81], v[138:139]
	v_pk_add_f32 v[40:41], v[40:41], v[144:145]
	v_pk_add_f32 v[80:81], v[80:81], v[142:143]
	v_pk_add_f32 v[40:41], v[40:41], v[148:149]
	v_pk_add_f32 v[80:81], v[80:81], v[146:147]
	s_nop 0
	v_pk_add_f32 v[80:81], v[80:81], v[150:151]
	s_nop 0
	v_pk_add_f32 v[62:63], v[80:81], v[62:63]
	v_pk_add_f32 v[40:41], v[40:41], v[152:153]
	v_mul_f32_e32 v42, 0x3d372713, v62
	v_mul_f32_e32 v42, v62, v42
	v_fma_f32 v42, v62, v42, v62
	v_mul_f32_e32 v42, 0x3f4c422a, v42
	v_mul_f32_e32 v42, 0xc038aa3b, v42
	v_pk_add_f32 v[40:41], v[40:41], v[64:65]
	v_mov_b32_e32 v64, v62
	v_exp_f32_e32 v62, v42
	v_mov_b32_e32 v72, v63
	v_pk_add_f32 v[86:87], v[88:89], 0 op_sel_hi:[1,0]
	v_mov_b32_e32 v65, v40
	v_add_f32_e32 v42, 1.0, v62
	v_rcp_f32_e32 v70, v42
	v_mul_f32_e32 v42, 0x3d372713, v63
	v_mul_f32_e32 v42, v63, v42
	v_fmac_f32_e32 v63, v63, v42
	v_mul_f32_e32 v42, 0x3f4c422a, v63
	v_mul_f32_e32 v42, 0xc038aa3b, v42
	v_exp_f32_e32 v80, v42
	v_mov_b32_e32 v73, v41
	v_pk_add_f32 v[86:87], v[86:87], v[92:93]
	v_pk_add_f32 v[84:85], v[90:91], 0 op_sel_hi:[1,0]
	v_add_f32_e32 v42, 1.0, v80
	v_rcp_f32_e32 v88, v42
	v_mul_f32_e32 v42, 0x3d372713, v40
	v_mul_f32_e32 v42, v40, v42
	v_fma_f32 v40, v40, v42, v40
	v_mul_f32_e32 v40, 0x3f4c422a, v40
	v_mul_f32_e32 v40, 0xc038aa3b, v40
	v_exp_f32_e32 v63, v40
	v_pk_add_f32 v[86:87], v[86:87], v[96:97]
	v_pk_add_f32 v[84:85], v[84:85], v[94:95]
	v_pk_add_f32 v[86:87], v[86:87], v[100:101]
	v_add_f32_e32 v40, 1.0, v63
	v_rcp_f32_e32 v71, v40
	v_mul_f32_e32 v40, 0x3d372713, v41
	v_mul_f32_e32 v40, v41, v40
	v_fmac_f32_e32 v41, v41, v40
	v_mul_f32_e32 v40, 0x3f4c422a, v41
	v_mul_f32_e32 v40, 0xc038aa3b, v40
	v_exp_f32_e32 v81, v40
	v_pk_add_f32 v[86:87], v[86:87], v[104:105]
	v_pk_add_f32 v[90:91], v[62:63], 1.0 op_sel_hi:[1,0] neg_lo:[1,0] neg_hi:[1,0]
	v_pk_add_f32 v[86:87], v[86:87], v[108:109]
	v_add_f32_e32 v42, 1.0, v81
	v_pk_add_f32 v[86:87], v[86:87], v[112:113]
	v_rcp_f32_e32 v89, v42
	v_pk_add_f32 v[86:87], v[86:87], v[116:117]
	v_pk_mul_f32 v[62:63], v[64:65], 0.5 op_sel_hi:[1,0]
	v_pk_add_f32 v[34:35], v[86:87], v[34:35]
	v_pk_fma_f32 v[64:65], v[90:91], v[70:71], 1.0 op_sel_hi:[1,1,0]
	v_pk_add_f32 v[40:41], v[80:81], 1.0 op_sel_hi:[1,0] neg_lo:[1,0] neg_hi:[1,0]
	v_mul_f32_e32 v42, 0x3d372713, v34
	v_pk_mul_f32 v[62:63], v[62:63], v[64:65]
	v_pk_mul_f32 v[64:65], v[72:73], 0.5 op_sel_hi:[1,0]
	v_pk_fma_f32 v[40:41], v[40:41], v[88:89], 1.0 op_sel_hi:[1,1,0]
	v_mul_f32_e32 v42, v34, v42
	v_pk_mul_f32 v[40:41], v[64:65], v[40:41]
	v_mov_b32_e32 v64, v34
	v_fma_f32 v34, v34, v42, v34
	v_mul_f32_e32 v34, 0x3f4c422a, v34
	v_mul_f32_e32 v34, 0xc038aa3b, v34
	v_exp_f32_e32 v34, v34
	v_mov_b32_e32 v68, v35
	v_pk_add_f32 v[84:85], v[84:85], v[98:99]
	v_add_f32_e32 v42, 1.0, v34
	v_rcp_f32_e32 v66, v42
	v_mul_f32_e32 v42, 0x3d372713, v35
	v_mul_f32_e32 v42, v35, v42
	v_fmac_f32_e32 v35, v35, v42
	v_mul_f32_e32 v35, 0x3f4c422a, v35
	v_pk_add_f32 v[84:85], v[84:85], v[102:103]
	v_mul_f32_e32 v35, 0xc038aa3b, v35
	v_pk_add_f32 v[84:85], v[84:85], v[106:107]
	v_exp_f32_e32 v70, v35
	v_pk_add_f32 v[84:85], v[84:85], v[110:111]
	v_lshl_add_u64 v[102:103], v[76:77], 0, s[22:23]
	v_pk_add_f32 v[84:85], v[84:85], v[114:115]
	v_add_f32_e32 v35, 1.0, v70
	v_pk_add_f32 v[84:85], v[84:85], v[118:119]
	v_rcp_f32_e32 v72, v35
	v_pk_add_f32 v[36:37], v[84:85], v[36:37]
	v_lshl_add_u64 v[118:119], v[76:77], 0, s[30:31]
	v_mul_f32_e32 v35, 0x3d372713, v36
	v_mul_f32_e32 v35, v36, v35
	v_mov_b32_e32 v65, v36
	v_fma_f32 v35, v36, v35, v36
	v_mul_f32_e32 v36, 0x3d372713, v37
	v_mul_f32_e32 v36, v37, v36
	v_mov_b32_e32 v69, v37
	v_mul_f32_e32 v35, 0x3f4c422a, v35
	v_fmac_f32_e32 v37, v37, v36
	v_mul_f32_e32 v35, 0xc038aa3b, v35
	v_mul_f32_e32 v36, 0x3f4c422a, v37
	v_exp_f32_e32 v35, v35
	v_mul_f32_e32 v36, 0xc038aa3b, v36
	v_exp_f32_e32 v71, v36
	v_pk_add_f32 v[80:81], v[34:35], 1.0 op_sel_hi:[1,0] neg_lo:[1,0] neg_hi:[1,0]
	v_add_f32_e32 v34, 1.0, v35
	v_rcp_f32_e32 v67, v34
	v_add_f32_e32 v42, 1.0, v71
	v_rcp_f32_e32 v73, v42
	v_pk_mul_f32 v[34:35], v[64:65], 0.5 op_sel_hi:[1,0]
	v_pk_fma_f32 v[64:65], v[80:81], v[66:67], 1.0 op_sel_hi:[1,1,0]
	v_pk_add_f32 v[36:37], v[70:71], 1.0 op_sel_hi:[1,0] neg_lo:[1,0] neg_hi:[1,0]
	v_pk_mul_f32 v[34:35], v[34:35], v[64:65]
	v_pk_mul_f32 v[64:65], v[68:69], 0.5 op_sel_hi:[1,0]
	v_pk_fma_f32 v[36:37], v[36:37], v[72:73], 1.0 op_sel_hi:[1,1,0]
	v_bfe_u32 v66, v40, 16, 1
	v_pk_mul_f32 v[36:37], v[64:65], v[36:37]
	v_bfe_u32 v65, v41, 16, 1
	v_bfe_u32 v42, v37, 16, 1
	v_bfe_u32 v64, v36, 16, 1
	v_add3_u32 v40, v40, v66, s50
	v_add3_u32 v41, v41, v65, s50
	v_add3_u32 v36, v36, v64, s50
	v_add3_u32 v37, v37, v42, s50
	v_bfe_u32 v42, v62, 16, 1
	v_bfe_u32 v64, v63, 16, 1
	v_bfe_u32 v65, v34, 16, 1
	v_bfe_u32 v66, v35, 16, 1
	v_add3_u32 v35, v35, v66, s50
	v_add3_u32 v34, v34, v65, s50
	v_add3_u32 v63, v63, v64, s50
	v_add3_u32 v42, v62, v42, s50
	v_lshrrev_b32_e32 v42, 16, v42
	v_lshrrev_b32_e32 v62, 16, v63
	v_lshrrev_b32_e32 v34, 16, v34
	v_lshrrev_b32_e32 v35, 16, v35
	v_and_or_b32 v37, v37, s51, v35
	v_and_or_b32 v36, v36, s51, v34
	v_and_or_b32 v35, v41, s51, v62
	v_and_or_b32 v34, v40, s51, v42
	v_lshl_add_u64 v[56:57], v[56:57], 0, s[40:41]
	s_nop 1
	v_mfma_f32_16x16x32_bf16 v[6:9], v[34:37], v[154:157], v[6:9]
	v_mfma_f32_16x16x32_bf16 v[2:5], v[34:37], v[158:161], v[2:5]
	v_mfma_f32_16x16x32_bf16 v[30:33], v[34:37], v[162:165], v[30:33]
	v_mfma_f32_16x16x32_bf16 v[26:29], v[34:37], v[166:169], v[26:29]
	v_mfma_f32_16x16x32_bf16 v[22:25], v[34:37], v[170:173], v[22:25]
	v_mfma_f32_16x16x32_bf16 v[18:21], v[34:37], v[174:177], v[18:21]
	v_mfma_f32_16x16x32_bf16 v[14:17], v[34:37], v[178:181], v[14:17]
	v_mfma_f32_16x16x32_bf16 v[10:13], v[34:37], v[182:185], v[10:13]
	global_load_dwordx4 v[154:157], v[188:189], off offset:64
	s_nop 0
	global_load_dwordx4 v[158:161], v[190:191], off offset:64
	s_nop 0
	global_load_dwordx4 v[162:165], v[192:193], off offset:64
	s_nop 0
	global_load_dwordx4 v[166:169], v[194:195], off offset:64
	s_nop 0
	global_load_dwordx4 v[170:173], v[196:197], off offset:64
	s_nop 0
	global_load_dwordx4 v[174:177], v[198:199], off offset:64
	s_nop 0
	global_load_dwordx4 v[178:181], v[200:201], off offset:64
	s_nop 0
	global_load_dwordx4 v[182:185], v[202:203], off offset:64
	s_nop 0
	global_load_dwordx4 v[34:37], v[38:39], off offset:16
	global_load_dwordx4 v[86:89], v[38:39], off
	s_nop 0
	global_load_dwordx4 v[38:41], v[82:83], off offset:16
	global_load_dwordx4 v[90:93], v[82:83], off
	v_lshl_add_u64 v[82:83], v[76:77], 0, s[20:21]
	global_load_dwordx4 v[94:97], v[78:79], off offset:128
	global_load_dwordx4 v[98:101], v[82:83], off offset:16
	s_nop 0
	global_load_dwordx4 v[126:129], v[78:79], off offset:1152
	s_nop 0
	global_load_dwordx4 v[130:133], v[78:79], off offset:2176
	s_nop 0
	global_load_dwordx4 v[134:137], v[78:79], off offset:3200
	s_nop 0
	global_load_dwordx4 v[138:141], v[74:75], off offset:128
	s_nop 0
	global_load_dwordx4 v[142:145], v[74:75], off offset:1152
	s_nop 0
	global_load_dwordx4 v[146:149], v[74:75], off offset:2176
	s_nop 0
	global_load_dwordx4 v[150:153], v[74:75], off offset:3200
	s_nop 0
	global_load_dwordx4 v[102:105], v[102:103], off offset:16
	s_nop 0
	v_lshl_add_u64 v[204:205], v[76:77], 0, s[24:25]
	global_load_dwordx4 v[204:207], v[204:205], off offset:16
	s_nop 0
	v_lshl_add_u64 v[208:209], v[76:77], 0, s[26:27]
	global_load_dwordx4 v[208:211], v[208:209], off offset:16
	s_nop 0
	v_lshl_add_u64 v[212:213], v[76:77], 0, s[28:29]
	global_load_dwordx4 v[212:215], v[212:213], off offset:16
	s_nop 0
	global_load_dwordx4 v[118:121], v[118:119], off offset:16
	s_nop 0
	global_load_dwordx4 v[122:125], v[122:123], off offset:16
	s_nop 0
	v_lshl_add_u64 v[216:217], v[76:77], 0, s[36:37]
	global_load_dwordx4 v[216:219], v[216:217], off offset:16
	s_waitcnt vmcnt(0)
	v_pk_add_f32 v[34:35], v[34:35], v[38:39]
	v_pk_add_f32 v[86:87], v[86:87], v[90:91]
	v_pk_add_f32 v[82:83], v[96:97], 0 op_sel_hi:[1,0]
	v_pk_add_f32 v[106:107], v[94:95], 0 op_sel_hi:[1,0]
	v_pk_add_f32 v[88:89], v[88:89], v[92:93]
	v_pk_add_f32 v[36:37], v[36:37], v[40:41]
	v_pk_add_f32 v[110:111], v[106:107], v[126:127]
	v_pk_add_f32 v[82:83], v[82:83], v[128:129]
	v_pk_add_f32 v[114:115], v[110:111], v[130:131]
	v_pk_add_f32 v[82:83], v[82:83], v[132:133]
	s_nop 0
	v_pk_add_f32 v[78:79], v[82:83], v[136:137]
	v_pk_add_f32 v[82:83], v[114:115], v[134:135]
	v_pk_add_f32 v[78:79], v[78:79], v[140:141]
	v_pk_add_f32 v[82:83], v[82:83], v[138:139]
	v_pk_add_f32 v[78:79], v[78:79], v[144:145]
	v_pk_add_f32 v[82:83], v[82:83], v[142:143]
	s_nop 0
	v_pk_add_f32 v[82:83], v[82:83], v[146:147]
	v_pk_add_f32 v[78:79], v[78:79], v[148:149]
	v_pk_add_f32 v[74:75], v[82:83], v[150:151]
	s_nop 0
	v_pk_add_f32 v[74:75], v[74:75], v[86:87]
	v_pk_add_f32 v[76:77], v[78:79], v[152:153]
	v_mul_f32_e32 v42, 0x3d372713, v74
	v_mul_f32_e32 v42, v74, v42
	v_fma_f32 v42, v74, v42, v74
	v_mul_f32_e32 v42, 0x3f4c422a, v42
	v_mul_f32_e32 v42, 0xc038aa3b, v42
	v_mov_b32_e32 v86, v74
	v_exp_f32_e32 v74, v42
	v_pk_add_f32 v[76:77], v[76:77], v[88:89]
	v_mov_b32_e32 v90, v75
	v_pk_add_f32 v[82:83], v[98:99], 0 op_sel_hi:[1,0]
	v_add_f32_e32 v42, 1.0, v74
	v_rcp_f32_e32 v88, v42
	v_mul_f32_e32 v42, 0x3d372713, v75
	v_mul_f32_e32 v42, v75, v42
	v_fmac_f32_e32 v75, v75, v42
	v_mul_f32_e32 v42, 0x3f4c422a, v75
	v_pk_add_f32 v[82:83], v[82:83], v[102:103]
	v_mul_f32_e32 v42, 0xc038aa3b, v42
	v_pk_add_f32 v[82:83], v[82:83], v[204:205]
	v_exp_f32_e32 v92, v42
	v_pk_add_f32 v[82:83], v[82:83], v[208:209]
	v_pk_add_f32 v[78:79], v[100:101], 0 op_sel_hi:[1,0]
	v_pk_add_f32 v[82:83], v[82:83], v[212:213]
	v_add_f32_e32 v42, 1.0, v92
	v_pk_add_f32 v[82:83], v[82:83], v[118:119]
	v_pk_add_f32 v[78:79], v[78:79], v[104:105]
	v_pk_add_f32 v[82:83], v[82:83], v[122:123]
	v_pk_add_f32 v[78:79], v[78:79], v[206:207]
	v_pk_add_f32 v[82:83], v[82:83], v[216:217]
	v_rcp_f32_e32 v94, v42
	v_mul_f32_e32 v42, 0x3d372713, v76
	v_mul_f32_e32 v42, v76, v42
	v_fma_f32 v42, v76, v42, v76
	v_mul_f32_e32 v42, 0x3f4c422a, v42
	v_mul_f32_e32 v42, 0xc038aa3b, v42
	v_exp_f32_e32 v75, v42
	v_pk_add_f32 v[78:79], v[78:79], v[210:211]
	v_mov_b32_e32 v91, v77
	v_pk_add_f32 v[78:79], v[78:79], v[214:215]
	v_add_f32_e32 v42, 1.0, v75
	v_rcp_f32_e32 v89, v42
	v_mul_f32_e32 v42, 0x3d372713, v77
	v_mul_f32_e32 v42, v77, v42
	v_fmac_f32_e32 v77, v77, v42
	v_mul_f32_e32 v42, 0x3f4c422a, v77
	v_pk_add_f32 v[78:79], v[78:79], v[120:121]
	v_mul_f32_e32 v42, 0xc038aa3b, v42
	v_pk_add_f32 v[34:35], v[82:83], v[34:35]
	v_pk_add_f32 v[78:79], v[78:79], v[124:125]
	v_exp_f32_e32 v93, v42
	v_mul_f32_e32 v41, 0x3d372713, v35
	v_pk_add_f32 v[78:79], v[78:79], v[218:219]
	v_mul_f32_e32 v41, v35, v41
	v_pk_add_f32 v[36:37], v[78:79], v[36:37]
	v_mov_b32_e32 v78, v35
	v_fmac_f32_e32 v35, v35, v41
	v_mul_f32_e32 v35, 0x3f4c422a, v35
	v_add_f32_e32 v42, 1.0, v93
	v_mul_f32_e32 v35, 0xc038aa3b, v35
	v_rcp_f32_e32 v95, v42
	v_exp_f32_e32 v82, v35
	v_mov_b32_e32 v87, v76
	v_pk_add_f32 v[96:97], v[74:75], 1.0 op_sel_hi:[1,0] neg_lo:[1,0] neg_hi:[1,0]
	v_pk_mul_f32 v[74:75], v[86:87], 0.5 op_sel_hi:[1,0]
	v_pk_fma_f32 v[86:87], v[96:97], v[88:89], 1.0 op_sel_hi:[1,1,0]
	v_pk_add_f32 v[76:77], v[92:93], 1.0 op_sel_hi:[1,0] neg_lo:[1,0] neg_hi:[1,0]
	v_pk_mul_f32 v[74:75], v[74:75], v[86:87]
	v_pk_mul_f32 v[86:87], v[90:91], 0.5 op_sel_hi:[1,0]
	v_pk_fma_f32 v[76:77], v[76:77], v[94:95], 1.0 op_sel_hi:[1,1,0]
	v_add_f32_e32 v35, 1.0, v82
	v_pk_mul_f32 v[76:77], v[86:87], v[76:77]
	v_mul_f32_e32 v40, 0x3d372713, v34
	v_rcp_f32_e32 v86, v35
	v_mul_f32_e32 v35, 0x3d372713, v36
	v_mul_f32_e32 v40, v34, v40
	v_mul_f32_e32 v35, v36, v35
	v_mov_b32_e32 v38, v34
	v_fma_f32 v34, v34, v40, v34
	v_fma_f32 v35, v36, v35, v36
	v_mul_f32_e32 v34, 0x3f4c422a, v34
	v_mul_f32_e32 v35, 0x3f4c422a, v35
	v_mul_f32_e32 v34, 0xc038aa3b, v34
	v_mul_f32_e32 v35, 0xc038aa3b, v35
	v_exp_f32_e32 v34, v34
	v_exp_f32_e32 v35, v35
	v_mov_b32_e32 v39, v36
	v_mul_f32_e32 v36, 0x3d372713, v37
	v_mul_f32_e32 v36, v37, v36
	v_mov_b32_e32 v79, v37
	v_fmac_f32_e32 v37, v37, v36
	v_add_f32_e32 v40, 1.0, v34
	v_pk_add_f32 v[88:89], v[34:35], 1.0 op_sel_hi:[1,0] neg_lo:[1,0] neg_hi:[1,0]
	v_add_f32_e32 v34, 1.0, v35
	v_mul_f32_e32 v36, 0x3f4c422a, v37
	v_rcp_f32_e32 v40, v40
	v_rcp_f32_e32 v41, v34
	v_mul_f32_e32 v36, 0xc038aa3b, v36
	v_exp_f32_e32 v83, v36
	v_pk_mul_f32 v[34:35], v[38:39], 0.5 op_sel_hi:[1,0]
	v_pk_fma_f32 v[38:39], v[88:89], v[40:41], 1.0 op_sel_hi:[1,1,0]
	v_bfe_u32 v41, v76, 16, 1
	v_pk_mul_f32 v[34:35], v[34:35], v[38:39]
	v_add_f32_e32 v38, 1.0, v83
	v_rcp_f32_e32 v87, v38
	v_pk_add_f32 v[36:37], v[82:83], 1.0 op_sel_hi:[1,0] neg_lo:[1,0] neg_hi:[1,0]
	v_pk_mul_f32 v[38:39], v[78:79], 0.5 op_sel_hi:[1,0]
	v_add3_u32 v41, v76, v41, s50
	v_pk_fma_f32 v[36:37], v[36:37], v[86:87], 1.0 op_sel_hi:[1,1,0]
	v_bfe_u32 v42, v34, 16, 1
	v_pk_mul_f32 v[36:37], v[38:39], v[36:37]
	v_bfe_u32 v76, v35, 16, 1
	v_bfe_u32 v38, v37, 16, 1
	v_bfe_u32 v39, v36, 16, 1
	v_add3_u32 v36, v36, v39, s50
	v_add3_u32 v37, v37, v38, s50
	v_bfe_u32 v38, v74, 16, 1
	v_bfe_u32 v39, v75, 16, 1
	v_bfe_u32 v40, v77, 16, 1
	v_add3_u32 v35, v35, v76, s50
	v_add3_u32 v34, v34, v42, s50
	v_add3_u32 v39, v75, v39, s50
	v_add3_u32 v38, v74, v38, s50
	v_add3_u32 v40, v77, v40, s50
	v_lshrrev_b32_e32 v38, 16, v38
	v_lshrrev_b32_e32 v39, 16, v39
	v_lshrrev_b32_e32 v34, 16, v34
	v_lshrrev_b32_e32 v35, 16, v35
	v_and_or_b32 v37, v37, s51, v35
	v_and_or_b32 v36, v36, s51, v34
	v_and_or_b32 v35, v40, s51, v39
	v_and_or_b32 v34, v41, s51, v38
	s_nop 1
	v_mfma_f32_16x16x32_bf16 v[6:9], v[34:37], v[154:157], v[6:9]
	v_mfma_f32_16x16x32_bf16 v[2:5], v[34:37], v[158:161], v[2:5]
	v_mfma_f32_16x16x32_bf16 v[30:33], v[34:37], v[162:165], v[30:33]
	v_mfma_f32_16x16x32_bf16 v[26:29], v[34:37], v[166:169], v[26:29]
	v_mfma_f32_16x16x32_bf16 v[22:25], v[34:37], v[170:173], v[22:25]
	v_mfma_f32_16x16x32_bf16 v[18:21], v[34:37], v[174:177], v[18:21]
	v_mfma_f32_16x16x32_bf16 v[14:17], v[34:37], v[178:181], v[14:17]
	v_mfma_f32_16x16x32_bf16 v[10:13], v[34:37], v[182:185], v[10:13]
	s_cbranch_scc0 .LBB0_511
	s_and_b32 s43, s4, 3
	s_lshl_b32 s4, s62, 2
	s_and_b32 s63, s4, 0x700
	v_or_b32_e32 v40, s42, v47
	v_bfe_u32 v34, v6, 16, 1
	s_cmpk_lt_u32 s62, 0x200
	v_add3_u32 v6, v6, v34, s50
	v_or_b32_e32 v34, s63, v40
	s_cselect_b32 s4, s60, 0x3c000000
	v_lshl_or_b32 v41, v34, 2, s43
	v_lshl_add_u64 v[38:39], v[44:45], 0, s[4:5]
	v_lshlrev_b32_e32 v42, 8, v41
	v_lshl_add_u64 v[34:35], v[38:39], 0, v[42:43]
	global_store_short_d16_hi v[34:35], v6, off
	v_bfe_u32 v6, v7, 16, 1
	v_add3_u32 v36, v7, v6, s50
	v_or_b32_e32 v6, 0x400, v42
	v_mov_b32_e32 v7, v43
	v_lshl_add_u64 v[6:7], v[38:39], 0, v[6:7]
	global_store_short_d16_hi v[6:7], v36, off
	v_bfe_u32 v36, v8, 16, 1
	v_or_b32_e32 v42, 0x800, v42
	v_add3_u32 v8, v8, v36, s50
	v_lshl_add_u64 v[36:37], v[38:39], 0, v[42:43]
	v_cmp_ne_u32_e32 vcc, s61, v40
	v_mov_b32_e32 v40, 0
	v_mov_b32_e32 v54, 0
	global_store_short_d16_hi v[36:37], v8, off
	s_and_saveexec_b64 s[42:43], vcc
	v_bfe_u32 v8, v9, 16, 1
	v_add3_u32 v8, v9, v8, s50
	v_lshrrev_b32_e32 v54, 16, v8
	s_or_b64 exec, exec, s[42:43]
	v_lshl_or_b32 v42, v41, 8, v49
	v_lshl_add_u64 v[8:9], v[38:39], 0, v[42:43]
	v_bfe_u32 v38, v2, 16, 1
	v_add3_u32 v2, v2, v38, s50
	global_store_short_d16_hi v[34:35], v2, off offset:32
	v_bfe_u32 v2, v3, 16, 1
	v_add3_u32 v2, v3, v2, s50
	global_store_short_d16_hi v[6:7], v2, off offset:32
	v_bfe_u32 v2, v4, 16, 1
	v_add3_u32 v2, v4, v2, s50
	global_store_short v[8:9], v54, off
	global_store_short_d16_hi v[36:37], v2, off offset:32
	s_and_saveexec_b64 s[42:43], vcc
	v_readlane_b32 s66, v254, 20
	v_readlane_b32 s67, v254, 21
	v_bfe_u32 v2, v5, 16, 1
	v_add3_u32 v2, v5, v2, s50
	v_lshrrev_b32_e32 v40, 16, v2
	s_or_b64 exec, exec, s[42:43]
	v_bfe_u32 v2, v30, 16, 1
	v_add3_u32 v2, v30, v2, s50
	global_store_short_d16_hi v[34:35], v2, off offset:64
	v_bfe_u32 v2, v31, 16, 1
	v_add3_u32 v2, v31, v2, s50
	global_store_short_d16_hi v[6:7], v2, off offset:64
	v_bfe_u32 v2, v32, 16, 1
	v_add3_u32 v2, v32, v2, s50
	global_store_short_d16_hi v[36:37], v2, off offset:64
	v_mov_b32_e32 v2, 0
	v_mov_b32_e32 v3, 0
	global_store_short v[8:9], v40, off offset:32
	s_and_saveexec_b64 s[42:43], vcc
	v_bfe_u32 v3, v33, 16, 1
	v_add3_u32 v3, v33, v3, s50
	v_lshrrev_b32_e32 v3, 16, v3
	s_or_b64 exec, exec, s[42:43]
	global_store_short v[8:9], v3, off offset:64
	v_bfe_u32 v3, v26, 16, 1
	v_add3_u32 v3, v26, v3, s50
	global_store_short_d16_hi v[34:35], v3, off offset:96
	v_bfe_u32 v3, v27, 16, 1
	v_add3_u32 v3, v27, v3, s50
	global_store_short_d16_hi v[6:7], v3, off offset:96
	v_bfe_u32 v3, v28, 16, 1
	v_add3_u32 v3, v28, v3, s50
	global_store_short_d16_hi v[36:37], v3, off offset:96
	s_and_saveexec_b64 s[42:43], vcc
	v_bfe_u32 v2, v29, 16, 1
	v_add3_u32 v2, v29, v2, s50
	v_lshrrev_b32_e32 v2, 16, v2
	s_or_b64 exec, exec, s[42:43]
	global_store_short v[8:9], v2, off offset:96
	v_bfe_u32 v2, v22, 16, 1
	v_add3_u32 v2, v22, v2, s50
	global_store_short_d16_hi v[34:35], v2, off offset:128
	v_bfe_u32 v2, v23, 16, 1
	v_add3_u32 v2, v23, v2, s50
	global_store_short_d16_hi v[6:7], v2, off offset:128
	v_bfe_u32 v2, v24, 16, 1
	v_add3_u32 v2, v24, v2, s50
	global_store_short_d16_hi v[36:37], v2, off offset:128
	v_mov_b32_e32 v2, 0
	v_mov_b32_e32 v3, 0
	s_and_saveexec_b64 s[42:43], vcc
	v_bfe_u32 v3, v25, 16, 1
	v_add3_u32 v3, v25, v3, s50
	v_lshrrev_b32_e32 v3, 16, v3
	s_or_b64 exec, exec, s[42:43]
	global_store_short v[8:9], v3, off offset:128
	v_bfe_u32 v3, v18, 16, 1
	v_add3_u32 v3, v18, v3, s50
	global_store_short_d16_hi v[34:35], v3, off offset:160
	v_bfe_u32 v3, v19, 16, 1
	v_add3_u32 v3, v19, v3, s50
	global_store_short_d16_hi v[6:7], v3, off offset:160
	v_bfe_u32 v3, v20, 16, 1
	v_add3_u32 v3, v20, v3, s50
	global_store_short_d16_hi v[36:37], v3, off offset:160
	s_and_saveexec_b64 s[42:43], vcc
	v_bfe_u32 v2, v21, 16, 1
	v_add3_u32 v2, v21, v2, s50
	v_lshrrev_b32_e32 v2, 16, v2
	s_or_b64 exec, exec, s[42:43]
	global_store_short v[8:9], v2, off offset:160
	v_bfe_u32 v2, v14, 16, 1
	v_add3_u32 v2, v14, v2, s50
	global_store_short_d16_hi v[34:35], v2, off offset:192
	v_bfe_u32 v2, v15, 16, 1
	v_add3_u32 v2, v15, v2, s50
	global_store_short_d16_hi v[6:7], v2, off offset:192
	v_bfe_u32 v2, v16, 16, 1
	v_add3_u32 v2, v16, v2, s50
	global_store_short_d16_hi v[36:37], v2, off offset:192
	v_mov_b32_e32 v2, 0
	v_mov_b32_e32 v3, 0
	s_and_saveexec_b64 s[42:43], vcc
	v_bfe_u32 v3, v17, 16, 1
	v_add3_u32 v3, v17, v3, s50
	v_lshrrev_b32_e32 v3, 16, v3
	s_or_b64 exec, exec, s[42:43]
	global_store_short v[8:9], v3, off offset:192
	v_bfe_u32 v3, v10, 16, 1
	v_add3_u32 v3, v10, v3, s50
	global_store_short_d16_hi v[34:35], v3, off offset:224
	v_bfe_u32 v3, v11, 16, 1
	v_add3_u32 v3, v11, v3, s50
	global_store_short_d16_hi v[6:7], v3, off offset:224
	v_bfe_u32 v3, v12, 16, 1
	v_add3_u32 v3, v12, v3, s50
	global_store_short_d16_hi v[36:37], v3, off offset:224
	s_and_saveexec_b64 s[42:43], vcc
	s_cbranch_execz .LBB0_509
	v_bfe_u32 v2, v13, 16, 1
	v_add3_u32 v2, v13, v2, s50
	v_lshrrev_b32_e32 v2, 16, v2
	s_branch .LBB0_509
